# attention tile loop: running max across lanes via v_permlane16/32_swap instead of two ds_bpermute round trips; prep phase LRU items rebalanced (class 1 groups 7->6 items, class 0 groups 26-31 2->3)
# speedup vs baseline: 1.0023x; 1.0023x over previous
; __device__ void phase_swa_mfma(const Params& p, int l, char* smem, int vb, int nvb, int pend, int oz) {
;     ...
;             u32x4 o1, o2;
; #pragma unroll
;             for (int w = 0; w < 4; ++w) {
;                 o1[w] = cvt_pk(x1[2 * w] * QSC, x1[2 * w + 1] * QSC);
;                 o2[w] = cvt_pk(x2[2 * w] * QSC, x2[2 * w + 1] * QSC);
;             }
;             qf[qt2][0] = __builtin_bit_cast(bf16x8, o1);
;             qf[qt2][1] = __builtin_bit_cast(bf16x8, o2);
;     ...
;                 *(u32x4*)(Kl + fr * LS + 8 * fj) = o1;
;                 *(u32x4*)(Kl + fr * LS + 32 + 8 * fj) = o2;
;                 *(u32x4*)(Vl + fr * LS + 8 * fj) = v0;
;                 *(u32x4*)(Vl + fr * LS + 32 + 8 * fj) = v1;
;             }
;             __syncthreads();
;             if (ti + 1 < nloc + 4) SWA_PREFETCH(ti + 1)
;             f32x4 st[4][2];
; #pragma unroll
;             for (int km = 0; km < 4; ++km) {
;                 bf16x8 ka[2];
; #pragma unroll
;                 for (int ks = 0; ks < 2; ++ks) ka[ks] = *(const bf16x8*)(Kl + (16 * km + li) * LS + 32 * ks + 8 * g);
; #pragma unroll
;                 for (int qt2 = 0; qt2 < 2; ++qt2) {
;                     f32x4 acc = {0.f, 0.f, 0.f, 0.f};
; #pragma unroll
;                     for (int ks = 0; ks < 2; ++ks) acc = MFMA32(ka[ks], qf[qt2][ks], acc);
;                     st[km][qt2] = acc;
;                 }
;             }
;             if (edge) {
; #pragma unroll
;                 for (int qt2 = 0; qt2 < 2; ++qt2) {
;                     const int tq = qt * 64 + 32 * qsub + 16 * qt2 + li;
; #pragma unroll
;                     for (int km = 0; km < 4; ++km)
; #pragma unroll
;                         for (int r = 0; r < 4; ++r) {
;                             int dlt = ktile * 64 + 16 * km + 4 * g + r - tq;
;                             dlt = dlt < 0 ? -dlt : dlt;
;                             st[km][qt2][r] = (dlt <= 128 && !oob) ? st[km][qt2][r] : -1e30f;
;                         }
;                 }
;             }
;             bf16x8 pf[2][2];
; #pragma unroll
;             for (int qt2 = 0; qt2 < 2; ++qt2) {
;                 float mx = st[0][qt2][0];
; #pragma unroll
;                 for (int km = 0; km < 4; ++km)
; #pragma unroll
;                     for (int r = 0; r < 4; ++r) mx = fmaxf(mx, st[km][qt2][r]);
;                 mx = fmaxf(mx, __shfl_xor(mx, 16));
.LBB0_191:
	s_add_i32 s21, s81, 4
	s_sub_i32 s3, 1, s81
	s_add_i32 s24, s57, -1
	s_cmp_gt_u32 s24, 31
	s_cselect_b32 s26, s57, s24
	s_and_b64 s[24:25], s[40:41], exec
	s_cselect_b32 s3, s26, s3
	s_waitcnt vmcnt(3)
	ds_write_b128 v161, v[16:19]
	s_waitcnt vmcnt(1)
	ds_write_b128 v161, v[12:15] offset:64
	ds_write_b128 v161, v[4:7] offset:9216
	s_waitcnt vmcnt(0)
	ds_write_b128 v161, v[8:11] offset:9280
	v_lshl_or_b32 v4, s3, 6, v160
	v_ashrrev_i32_e32 v5, 31, v4
	v_lshl_add_u64 v[4:5], s[42:43], 0, v[4:5]
	v_mov_b64_e32 v[6:7], s[34:35]
	v_mad_u64_u32 v[6:7], s[24:25], v4, s92, v[6:7]
	v_mad_i32_i24 v7, v5, s92, v7
	s_lshl_b32 s96, s2, 1
	s_mov_b32 s4, 0x3e38aa3b
	v_lshl_add_u64 v[4:5], v[6:7], 0, s[96:97]
	v_pk_mul_f32 v[24:25], v[24:25], s[4:5] op_sel_hi:[1,0]
	v_pk_mul_f32 v[22:23], v[22:23], s[4:5] op_sel_hi:[1,0]
	v_pk_mul_f32 v[32:33], v[32:33], s[4:5] op_sel_hi:[1,0]
	v_pk_mul_f32 v[30:31], v[30:31], s[4:5] op_sel_hi:[1,0]
	v_lshl_add_u64 v[4:5], v[4:5], 0, v[2:3]
	s_mov_b64 s[2:3], 0x1600
	v_pk_mov_b32 v[24:25], v[24:25], v[24:25] op_sel:[1,0]
	v_pk_mov_b32 v[22:23], v[22:23], v[22:23] op_sel:[1,0]
	v_pk_mov_b32 v[32:33], v[32:33], v[32:33] op_sel:[1,0]
	v_pk_mov_b32 v[30:31], v[30:31], v[30:31] op_sel:[1,0]
	v_lshl_add_u64 v[6:7], v[4:5], 0, s[2:3]
	s_mov_b64 s[2:3], 0x1700
	v_pk_mul_f32 v[20:21], v[20:21], s[4:5] op_sel_hi:[1,0]
	v_cvt_pk_bf16_f32 v24, v24, v25
	v_pk_mul_f32 v[50:51], v[50:51], s[4:5] op_sel_hi:[1,0]
	v_cvt_pk_bf16_f32 v25, v22, v23
	v_pk_mul_f32 v[22:23], v[48:49], s[4:5] op_sel_hi:[1,0]
	v_pk_mul_f32 v[26:27], v[26:27], s[4:5] op_sel_hi:[1,0]
	v_pk_mul_f32 v[46:47], v[46:47], s[4:5] op_sel_hi:[1,0]
	v_pk_mul_f32 v[44:45], v[44:45], s[4:5] op_sel_hi:[1,0]
	v_pk_mul_f32 v[28:29], v[28:29], s[4:5] op_sel_hi:[1,0]
	v_cvt_pk_bf16_f32 v32, v32, v33
	v_pk_mul_f32 v[42:43], v[42:43], s[4:5] op_sel_hi:[1,0]
	v_cvt_pk_bf16_f32 v33, v30, v31
	v_pk_mul_f32 v[30:31], v[40:41], s[4:5] op_sel_hi:[1,0]
	v_pk_mul_f32 v[34:35], v[34:35], s[4:5] op_sel_hi:[1,0]
	v_pk_mul_f32 v[38:39], v[38:39], s[4:5] op_sel_hi:[1,0]
	v_pk_mul_f32 v[36:37], v[36:37], s[4:5] op_sel_hi:[1,0]
	v_lshl_add_u64 v[8:9], v[4:5], 0, s[2:3]
	v_add_co_u32_e32 v4, vcc, s22, v4
	v_pk_mov_b32 v[20:21], v[20:21], v[20:21] op_sel:[1,0]
	v_pk_mov_b32 v[50:51], v[50:51], v[50:51] op_sel:[1,0]
	v_pk_mov_b32 v[22:23], v[22:23], v[22:23] op_sel:[1,0]
	v_pk_mov_b32 v[26:27], v[26:27], v[26:27] op_sel:[1,0]
	v_pk_mov_b32 v[46:47], v[46:47], v[46:47] op_sel:[1,0]
	v_pk_mov_b32 v[44:45], v[44:45], v[44:45] op_sel:[1,0]
	v_pk_mov_b32 v[28:29], v[28:29], v[28:29] op_sel:[1,0]
	v_pk_mov_b32 v[42:43], v[42:43], v[42:43] op_sel:[1,0]
	v_pk_mov_b32 v[30:31], v[30:31], v[30:31] op_sel:[1,0]
	v_pk_mov_b32 v[34:35], v[34:35], v[34:35] op_sel:[1,0]
	v_pk_mov_b32 v[38:39], v[38:39], v[38:39] op_sel:[1,0]
	v_pk_mov_b32 v[36:37], v[36:37], v[36:37] op_sel:[1,0]
	v_addc_co_u32_e32 v5, vcc, 0, v5, vcc
	v_cvt_pk_bf16_f32 v20, v20, v21
	v_cvt_pk_bf16_f32 v21, v50, v51
	v_cvt_pk_bf16_f32 v22, v22, v23
	v_cvt_pk_bf16_f32 v26, v26, v27
	v_cvt_pk_bf16_f32 v23, v46, v47
	v_cvt_pk_bf16_f32 v27, v44, v45
	v_cvt_pk_bf16_f32 v28, v28, v29
	v_cvt_pk_bf16_f32 v29, v42, v43
	v_cvt_pk_bf16_f32 v30, v30, v31
	v_cvt_pk_bf16_f32 v34, v34, v35
	v_cvt_pk_bf16_f32 v31, v38, v39
	v_cvt_pk_bf16_f32 v35, v36, v37
	s_waitcnt lgkmcnt(0)
	s_barrier
	global_load_dwordx4 v[36:39], v[4:5], off offset:1536
	global_load_dwordx4 v[40:43], v[6:7], off offset:64
	global_load_dwordx4 v[44:47], v[4:5], off offset:1792
	global_load_dwordx4 v[48:51], v[8:9], off offset:64
	ds_read_b128 v[4:7], v167
	ds_read_b128 v[8:11], v167 offset:64
	s_waitcnt lgkmcnt(1)
	v_mfma_f32_16x16x32_bf16 v[12:15], v[4:7], v[28:31], 0
	s_mov_b32 s2, 0xf149f2ca
	s_mov_b32 s24, 0
	v_mfma_f32_16x16x32_bf16 v[4:7], v[4:7], v[20:23], 0
	s_waitcnt lgkmcnt(0)
	v_mfma_f32_16x16x32_bf16 v[14:17], v[8:11], v[32:35], v[12:15]
	v_mfma_f32_16x16x32_bf16 v[4:7], v[8:11], v[24:27], v[4:7]
	ds_read_b128 v[8:11], v167 offset:2304
	ds_read_b128 v[52:55], v167 offset:2368
	s_nop 4
	v_max_f32_e32 v12, v15, v15
	v_max_f32_e32 v13, v14, v14
	s_waitcnt lgkmcnt(1)
	v_mfma_f32_16x16x32_bf16 v[56:59], v[8:11], v[28:31], 0
	v_max_f32_e32 v12, v13, v12
	v_max3_f32 v12, v12, v16, v17
	v_mfma_f32_16x16x32_bf16 v[8:11], v[8:11], v[20:23], 0
	s_waitcnt lgkmcnt(0)
	v_mfma_f32_16x16x32_bf16 v[56:59], v[52:55], v[32:35], v[56:59]
	v_mfma_f32_16x16x32_bf16 v[8:11], v[52:55], v[24:27], v[8:11]
	ds_read_b128 v[52:55], v167 offset:4608
	ds_read_b128 v[60:63], v167 offset:4672
	s_nop 4
	v_max3_f32 v12, v12, v56, v57
	v_max3_f32 v12, v12, v58, v59
	s_waitcnt lgkmcnt(1)
	v_mfma_f32_16x16x32_bf16 v[64:67], v[52:55], v[28:31], 0
	v_mfma_f32_16x16x32_bf16 v[52:55], v[52:55], v[20:23], 0
	s_waitcnt lgkmcnt(0)
	v_mfma_f32_16x16x32_bf16 v[64:67], v[60:63], v[32:35], v[64:67]
	v_mfma_f32_16x16x32_bf16 v[60:63], v[60:63], v[24:27], v[52:55]
	s_nop 4
	ds_read_b128 v[52:55], v167 offset:6912
	ds_read_b128 v[68:71], v167 offset:6976
	v_max3_f32 v12, v12, v64, v65
	v_max3_f32 v12, v12, v66, v67
	s_waitcnt lgkmcnt(1)
	v_mfma_f32_16x16x32_bf16 v[72:75], v[52:55], v[28:31], 0
	s_waitcnt lgkmcnt(0)
	v_mfma_f32_16x16x32_bf16 v[72:75], v[68:71], v[32:35], v[72:75]
	v_mfma_f32_16x16x32_bf16 v[52:55], v[52:55], v[20:23], 0
	v_mfma_f32_16x16x32_bf16 v[68:71], v[68:71], v[24:27], v[52:55]
	s_nop 5
	v_max3_f32 v12, v12, v72, v73
	v_max3_f32 v12, v12, v74, v75
	v_mov_b32_e32 v13, v12
	v_mov_b32_e32 v238, v12
	s_nop 1
	v_permlane16_swap_b32 v13, v238
	v_max_f32_e32 v13, v13, v238
	s_waitcnt lgkmcnt(0)
	v_max_f32_e32 v13, v13, v13
	v_max_f32_e32 v12, v12, v13
	v_mov_b32_e32 v13, v12
	v_mov_b32_e32 v238, v12
	s_nop 1
	v_permlane32_swap_b32 v13, v238
	v_max_f32_e32 v13, v13, v238
	s_waitcnt lgkmcnt(0)
; __device__ __forceinline__ float fexp2(float x) { return __builtin_amdgcn_exp2f(x); }
; #define MFMA32(a, b, c) __builtin_amdgcn_mfma_f32_16x16x32_bf16((a), (b), (c), 0, 0, 0)
; __device__ __forceinline__ bf16x8 cat8(bf16x4 a, bf16x4 b) { return __builtin_shufflevector(a, b, 0, 1, 2, 3, 4, 5, 6, 7); }
; __device__ void phase_swa_mfma(const Params& p, int l, char* smem, int vb, int nvb, int pend, int oz) {
;     ...
;                 const float mn = fmaxf(m[qt2], mx);
;                 const float sc = fexp2(m[qt2] - mn);
;                 m[qt2] = mn;
;                 float ps = 0.f;
; #pragma unroll
;                 for (int km = 0; km < 4; ++km)
; #pragma unroll
;                     for (int r = 0; r < 4; ++r) {
;                         const float pv = fexp2(st[km][qt2][r] - mn);
;                         st[km][qt2][r] = pv;
;                         ps += pv;
;                     }
;                 lsum[qt2] = lsum[qt2] * sc + ps;
; #pragma unroll
;                 for (int dt = 0; dt < 4; ++dt) O[dt][qt2] = O[dt][qt2] * sc;
;                 pf[qt2][0] = pack8(st[0][qt2], st[1][qt2]);
;                 pf[qt2][1] = pack8(st[2][qt2], st[3][qt2]);
;             }
; #pragma unroll
;             for (int dt = 0; dt < 4; ++dt)
; #pragma unroll
;                 for (int ks = 0; ks < 2; ++ks) {
;                     const bf16x8 va = cat8(lds_tr(Vl + (32 * ks + 4 * g + q4) * LS + 16 * dt + 4 * p4),
;                                            lds_tr(Vl + (32 * ks + 16 + 4 * g + q4) * LS + 16 * dt + 4 * p4));
; #pragma unroll
;                     for (int qt2 = 0; qt2 < 2; ++qt2) O[dt][qt2] = MFMA32(va, pf[qt2][ks], O[dt][qt2]);
;                 }
	v_max3_f32 v105, v12, v13, s2
	v_sub_f32_e32 v13, v14, v105
	v_sub_f32_e32 v14, v15, v105
	v_exp_f32_e32 v15, v14
	v_sub_f32_e32 v14, v16, v105
	v_exp_f32_e32 v137, v14
	v_sub_f32_e32 v14, v17, v105
	v_exp_f32_e32 v169, v14
	v_sub_f32_e32 v14, v56, v105
	v_exp_f32_e32 v171, v14
	v_sub_f32_e32 v14, v57, v105
	v_exp_f32_e32 v173, v14
	v_sub_f32_e32 v14, v58, v105
	v_exp_f32_e32 v135, v14
	v_sub_f32_e32 v14, v59, v105
	v_exp_f32_e32 v133, v14
	v_sub_f32_e32 v14, v64, v105
	v_exp_f32_e32 v131, v14
	v_sub_f32_e32 v14, v65, v105
	v_exp_f32_e32 v99, v14
	v_sub_f32_e32 v14, v66, v105
	v_exp_f32_e32 v97, v14
	v_sub_f32_e32 v14, v67, v105
	v_exp_f32_e32 v95, v14
	v_sub_f32_e32 v14, v72, v105
	v_exp_f32_e32 v93, v14
	v_sub_f32_e32 v14, v73, v105
	v_exp_f32_e32 v91, v14
	v_sub_f32_e32 v14, v74, v105
	v_sub_f32_e32 v12, 0xf149f2ca, v105
	v_exp_f32_e32 v89, v14
	v_sub_f32_e32 v14, v75, v105
	v_exp_f32_e32 v85, v14
	v_exp_f32_e32 v87, v12
	v_max_f32_e32 v12, v5, v5
	v_max_f32_e32 v14, v4, v4
	v_max_f32_e32 v12, v14, v12
	v_max3_f32 v12, v12, v6, v7
	v_max3_f32 v12, v12, v8, v9
	v_max3_f32 v12, v12, v10, v11
	v_max3_f32 v12, v12, v60, v61
	v_max3_f32 v12, v12, v62, v63
	v_max3_f32 v12, v12, v68, v69
	v_max3_f32 v12, v12, v70, v71
	v_mov_b32_e32 v14, v12
	v_mov_b32_e32 v238, v12
	s_nop 1
	v_permlane16_swap_b32 v14, v238
	v_max_f32_e32 v14, v14, v238
	v_exp_f32_e32 v13, v13
	v_cvt_pk_bf16_f32 v53, v137, v169
	v_cvt_pk_bf16_f32 v54, v171, v173
	v_cvt_pk_bf16_f32 v55, v135, v133
	s_waitcnt lgkmcnt(0)
	v_max_f32_e32 v14, v14, v14
	v_max_f32_e32 v12, v12, v14
	v_mov_b32_e32 v14, v12
	v_mov_b32_e32 v238, v12
	s_nop 1
	v_permlane32_swap_b32 v14, v238
	v_max_f32_e32 v14, v14, v238
	v_cvt_pk_bf16_f32 v52, v13, v15
	v_cvt_pk_bf16_f32 v16, v131, v99
	v_cvt_pk_bf16_f32 v17, v97, v95
	v_cvt_pk_bf16_f32 v18, v93, v91
	s_waitcnt lgkmcnt(0)
	v_max3_f32 v121, v12, v14, s2
	v_sub_f32_e32 v4, v4, v121
	v_exp_f32_e32 v12, v4
	v_sub_f32_e32 v4, v5, v121
	v_exp_f32_e32 v14, v4
	v_sub_f32_e32 v4, v6, v121
	v_exp_f32_e32 v136, v4
	v_sub_f32_e32 v4, v7, v121
	v_exp_f32_e32 v168, v4
	v_sub_f32_e32 v4, v8, v121
	v_exp_f32_e32 v170, v4
	v_sub_f32_e32 v4, v9, v121
	v_exp_f32_e32 v172, v4
	v_sub_f32_e32 v4, v10, v121
	v_exp_f32_e32 v134, v4
	v_sub_f32_e32 v4, v11, v121
	v_exp_f32_e32 v132, v4
	v_sub_f32_e32 v4, v60, v121
	v_exp_f32_e32 v130, v4
	v_sub_f32_e32 v4, v61, v121
	v_sub_f32_e32 v56, 0xf149f2ca, v121
	v_exp_f32_e32 v98, v4
	v_sub_f32_e32 v4, v62, v121
	v_exp_f32_e32 v96, v4
	v_sub_f32_e32 v4, v63, v121
	v_exp_f32_e32 v86, v56
	v_cvt_pk_bf16_f32 v72, v12, v14
	v_pk_add_f32 v[12:13], v[12:13], 0 op_sel_hi:[1,0]
	v_exp_f32_e32 v94, v4
	v_sub_f32_e32 v4, v68, v121
	v_pk_add_f32 v[12:13], v[14:15], v[12:13]
	v_exp_f32_e32 v92, v4
	v_sub_f32_e32 v4, v69, v121
	v_pk_add_f32 v[12:13], v[136:137], v[12:13]
	v_exp_f32_e32 v90, v4
	v_sub_f32_e32 v4, v70, v121
	v_pk_add_f32 v[12:13], v[168:169], v[12:13]
	v_exp_f32_e32 v88, v4
	v_sub_f32_e32 v4, v71, v121
	v_cvt_pk_bf16_f32 v73, v136, v168
	v_pk_add_f32 v[12:13], v[170:171], v[12:13]
	v_pk_mul_f32 v[168:169], v[86:87], 0 op_sel_hi:[1,0]
	v_exp_f32_e32 v84, v4
	v_cvt_pk_bf16_f32 v74, v170, v172
	v_cvt_pk_bf16_f32 v75, v134, v132
	ds_read_b64_tr_b16 v[58:59], v165 offset:11520
	ds_read_b64_tr_b16 v[56:57], v165 offset:9216
	ds_read_b64_tr_b16 v[4:5], v165 offset:9248
	ds_read_b64_tr_b16 v[60:61], v165 offset:13824
	ds_read_b64_tr_b16 v[62:63], v165 offset:16128
	ds_read_b64_tr_b16 v[6:7], v165 offset:11552
	ds_read_b64_tr_b16 v[138:139], v165 offset:13856
	ds_read_b64_tr_b16 v[140:141], v165 offset:16160
	ds_read_b64_tr_b16 v[142:143], v165 offset:9280
	ds_read_b64_tr_b16 v[144:145], v165 offset:11584
	ds_read_b64_tr_b16 v[8:9], v165 offset:13888
	ds_read_b64_tr_b16 v[10:11], v165 offset:16192
	ds_read_b64_tr_b16 v[80:81], v165 offset:9312
	ds_read_b64_tr_b16 v[82:83], v165 offset:11616
	ds_read_b64_tr_b16 v[76:77], v165 offset:13920
	ds_read_b64_tr_b16 v[78:79], v165 offset:16224
	v_pk_add_f32 v[136:137], v[172:173], v[12:13]
	v_mov_b32_e32 v172, v169
	v_mov_b32_e32 v173, v169
	v_mov_b32_e32 v174, v169
	v_mov_b32_e32 v175, v169
	v_mov_b32_e32 v169, v168
	v_mov_b32_e32 v170, v168
	v_mov_b32_e32 v171, v168
	s_waitcnt lgkmcnt(14)
	v_mfma_f32_16x16x32_bf16 v[12:15], v[56:59], v[52:55], v[172:175]
	v_cvt_pk_bf16_f32 v19, v89, v85
	v_cvt_pk_bf16_f32 v68, v130, v98
	v_cvt_pk_bf16_f32 v69, v96, v94
	v_mfma_f32_16x16x32_bf16 v[56:59], v[56:59], v[72:75], v[168:171]
	v_cvt_pk_bf16_f32 v70, v92, v90
	v_cvt_pk_bf16_f32 v71, v88, v84
	s_sub_i32 s2, 0, s81
	s_waitcnt lgkmcnt(11)
	v_mfma_f32_16x16x32_bf16 v[64:67], v[60:63], v[16:19], v[12:15]
	v_mfma_f32_16x16x32_bf16 v[12:15], v[60:63], v[68:71], v[56:59]
	s_waitcnt lgkmcnt(10)
	v_mfma_f32_16x16x32_bf16 v[56:59], v[4:7], v[52:55], v[172:175]
	v_mfma_f32_16x16x32_bf16 v[4:7], v[4:7], v[72:75], v[168:171]
	s_waitcnt lgkmcnt(8)
	v_mfma_f32_16x16x32_bf16 v[60:63], v[138:141], v[16:19], v[56:59]
	v_mfma_f32_16x16x32_bf16 v[4:7], v[138:141], v[68:71], v[4:7]
	s_waitcnt lgkmcnt(6)
	v_mfma_f32_16x16x32_bf16 v[56:59], v[142:145], v[52:55], v[172:175]
	v_mfma_f32_16x16x32_bf16 v[138:141], v[142:145], v[72:75], v[168:171]
	s_waitcnt lgkmcnt(2)
	v_mfma_f32_16x16x32_bf16 v[52:55], v[80:83], v[52:55], v[172:175]
	v_mfma_f32_16x16x32_bf16 v[72:75], v[80:83], v[72:75], v[168:171]
	v_mfma_f32_16x16x32_bf16 v[56:59], v[8:11], v[16:19], v[56:59]
	v_mfma_f32_16x16x32_bf16 v[8:11], v[8:11], v[68:71], v[138:141]
	s_waitcnt lgkmcnt(0)
	v_mfma_f32_16x16x32_bf16 v[52:55], v[76:79], v[16:19], v[52:55]
	v_mfma_f32_16x16x32_bf16 v[16:19], v[76:79], v[68:71], v[72:75]
	v_add_f32_e64 v68, v134, v136
	v_add_f32_e64 v69, v135, v137
	v_pk_add_f32 v[68:69], v[132:133], v[68:69]
	s_nop 0
	v_pk_add_f32 v[68:69], v[130:131], v[68:69]
	s_nop 0
	v_pk_add_f32 v[68:69], v[98:99], v[68:69]
	s_nop 0
	v_pk_add_f32 v[68:69], v[96:97], v[68:69]
	s_nop 0
	v_pk_add_f32 v[68:69], v[94:95], v[68:69]
	s_nop 0
	v_pk_add_f32 v[68:69], v[92:93], v[68:69]
	s_nop 0
	v_pk_add_f32 v[68:69], v[90:91], v[68:69]
	s_nop 0
	v_pk_add_f32 v[68:69], v[88:89], v[68:69]
	s_nop 0
	v_pk_add_f32 v[68:69], v[84:85], v[68:69]
	s_nop 0
	v_pk_fma_f32 v[130:131], v[86:87], 0, v[68:69] op_sel_hi:[1,0,1]

; __device__ __forceinline__ float fexp2(float x) { return __builtin_amdgcn_exp2f(x); }
; __device__ void phase_swa_mfma(const Params& p, int l, char* smem, int vb, int nvb, int pend, int oz) {
;     ...
;             for (int qt2 = 0; qt2 < 2; ++qt2) {
;                 float mx = st[0][qt2][0];
; #pragma unroll
;                 for (int km = 0; km < 4; ++km)
; #pragma unroll
;                     for (int r = 0; r < 4; ++r) mx = fmaxf(mx, st[km][qt2][r]);
;                 mx = fmaxf(mx, __shfl_xor(mx, 16));
;                 mx = fmaxf(mx, __shfl_xor(mx, 32));
;                 const float mn = fmaxf(m[qt2], mx);
;                 const float sc = fexp2(m[qt2] - mn);
;                 m[qt2] = mn;
;                 float ps = 0.f;
; #pragma unroll
;                 for (int km = 0; km < 4; ++km)
; #pragma unroll
;                     for (int r = 0; r < 4; ++r) {
;                         const float pv = fexp2(st[km][qt2][r] - mn);
;                         st[km][qt2][r] = pv;
;                         ps += pv;
;                     }
;                 lsum[qt2] = lsum[qt2] * sc + ps;
; #pragma unroll
;                 for (int dt = 0; dt < 4; ++dt) O[dt][qt2] = O[dt][qt2] * sc;
;                 pf[qt2][0] = pack8(st[0][qt2], st[1][qt2]);
;                 pf[qt2][1] = pack8(st[2][qt2], st[3][qt2]);
.LBB0_216:
	v_max_f32_e32 v127, v97, v97
	s_nop 0
	v_max_f32_e32 v132, v96, v96
	v_max_f32_e32 v127, v132, v127
	v_max3_f32 v127, v127, v98, v99
	v_max3_f32 v127, v127, v84, v85
	v_max3_f32 v127, v127, v86, v87
	v_max3_f32 v127, v127, v88, v89
	v_max3_f32 v127, v127, v90, v91
	v_max3_f32 v127, v127, v92, v93
	v_max3_f32 v127, v127, v94, v95
	v_mov_b32_e32 v132, v127
	v_mov_b32_e32 v238, v127
	s_nop 1
	v_permlane16_swap_b32 v132, v238
	v_max_f32_e32 v132, v132, v238
	s_add_i32 s24, s2, s3
	s_cmp_eq_u32 s24, 3
	s_waitcnt lgkmcnt(0)
	v_max_f32_e32 v132, v132, v132
	v_max_f32_e32 v127, v127, v132
	v_mov_b32_e32 v132, v127
	v_mov_b32_e32 v238, v127
	s_nop 1
	v_permlane32_swap_b32 v132, v238
	v_max_f32_e32 v132, v132, v238
	s_waitcnt lgkmcnt(0)
	v_max3_f32 v127, v105, v127, v132
	v_sub_f32_e32 v96, v96, v127
	v_exp_f32_e32 v96, v96
	v_sub_f32_e32 v97, v97, v127
	v_exp_f32_e32 v134, v97
	v_sub_f32_e32 v98, v98, v127
	v_add_f32_e32 v132, 0, v96
	v_exp_f32_e32 v98, v98
	v_sub_f32_e32 v99, v99, v127
	v_add_f32_e32 v97, v134, v132
	v_exp_f32_e32 v132, v99
	v_sub_f32_e32 v84, v84, v127
	v_exp_f32_e32 v136, v84
	v_sub_f32_e32 v85, v85, v127
	v_exp_f32_e32 v138, v85
	v_add_f32_e32 v97, v98, v97
	v_add_f32_e32 v97, v132, v97
	v_add_f32_e32 v84, v136, v97
	v_add_f32_e32 v145, v138, v84
	v_sub_f32_e32 v84, v86, v127
	v_exp_f32_e32 v97, v84
	v_sub_f32_e32 v84, v87, v127
	v_exp_f32_e32 v99, v84
	v_sub_f32_e32 v84, v88, v127
	v_exp_f32_e32 v133, v84
	v_sub_f32_e32 v84, v89, v127
	v_exp_f32_e32 v135, v84
	v_sub_f32_e32 v84, v90, v127
	v_exp_f32_e32 v137, v84
	v_sub_f32_e32 v84, v91, v127
	v_exp_f32_e32 v139, v84
	v_sub_f32_e32 v84, v92, v127
	v_exp_f32_e32 v141, v84
	v_sub_f32_e32 v84, v93, v127
	v_exp_f32_e32 v93, v84
	v_sub_f32_e32 v84, v94, v127
	v_max_f32_e32 v92, v81, v81
	v_max_f32_e32 v94, v80, v80
	v_max_f32_e32 v92, v94, v92
	v_max3_f32 v92, v92, v82, v83
	v_max3_f32 v92, v92, v68, v69
	v_max3_f32 v92, v92, v70, v71
	v_max3_f32 v92, v92, v72, v73
	v_max3_f32 v92, v92, v74, v75
	v_max3_f32 v92, v92, v76, v77
	v_max3_f32 v92, v92, v78, v79
	v_mov_b32_e32 v94, v92
	v_mov_b32_e32 v238, v92
	s_nop 1
	v_permlane16_swap_b32 v94, v238
	v_max_f32_e32 v94, v94, v238
	v_sub_f32_e32 v105, v105, v127
	v_exp_f32_e32 v146, v105
	v_cvt_pk_bf16_f32 v88, v96, v134
	v_cvt_pk_bf16_f32 v89, v98, v132
	s_waitcnt lgkmcnt(0)
	v_max_f32_e32 v94, v94, v94
	v_max_f32_e32 v92, v92, v94
	v_mov_b32_e32 v94, v92
	v_mov_b32_e32 v238, v92
	s_nop 1
	v_permlane32_swap_b32 v94, v238
	v_max_f32_e32 v94, v94, v238
	v_cvt_pk_bf16_f32 v90, v136, v138
	v_pk_mul_f32 v[66:67], v[66:67], v[146:147] op_sel_hi:[1,0]
	v_pk_mul_f32 v[64:65], v[64:65], v[146:147] op_sel_hi:[1,0]
	v_cvt_pk_bf16_f32 v91, v97, v99
	s_waitcnt lgkmcnt(0)
	v_max3_f32 v105, v121, v92, v94
	v_sub_f32_e32 v80, v80, v105
	v_exp_f32_e32 v80, v80
	v_sub_f32_e32 v81, v81, v105
	v_exp_f32_e32 v81, v81
	v_sub_f32_e32 v82, v82, v105
	v_exp_f32_e32 v82, v82
	v_sub_f32_e32 v83, v83, v105
	v_exp_f32_e32 v83, v83
	v_sub_f32_e32 v68, v68, v105
	v_add_f32_e32 v92, 0, v80
	v_exp_f32_e32 v168, v68
	v_sub_f32_e32 v69, v69, v105
	v_add_f32_e32 v92, v81, v92
	v_exp_f32_e32 v169, v69
	v_add_f32_e32 v92, v82, v92
	v_add_f32_e32 v92, v83, v92
	v_add_f32_e32 v68, v168, v92
	v_add_f32_e32 v144, v169, v68
	v_sub_f32_e32 v68, v70, v105
	v_exp_f32_e32 v96, v68
	v_sub_f32_e32 v68, v71, v105
	v_exp_f32_e32 v98, v68
	v_sub_f32_e32 v68, v72, v105
	v_exp_f32_e32 v132, v68
	v_sub_f32_e32 v68, v73, v105
	v_exp_f32_e32 v134, v68
	v_sub_f32_e32 v68, v74, v105
	v_exp_f32_e32 v136, v68
	v_sub_f32_e32 v68, v75, v105
	v_exp_f32_e32 v138, v68
	v_sub_f32_e32 v68, v76, v105
	v_exp_f32_e32 v140, v68
	v_sub_f32_e32 v68, v77, v105
	v_exp_f32_e32 v92, v68
	v_sub_f32_e32 v68, v78, v105
	v_sub_f32_e32 v121, v121, v105
	v_exp_f32_e32 v142, v68
	v_sub_f32_e32 v68, v79, v105
	v_exp_f32_e32 v94, v68
	v_exp_f32_e32 v68, v121
	v_cvt_pk_bf16_f32 v72, v80, v81
	ds_read_b64_tr_b16 v[78:79], v165 offset:11520
	ds_read_b64_tr_b16 v[76:77], v165 offset:9216
	ds_read_b64_tr_b16 v[80:81], v165 offset:9248
	v_pk_add_f32 v[70:71], v[96:97], v[144:145]
	v_mov_b32_e32 v69, v146
	v_pk_add_f32 v[70:71], v[98:99], v[70:71]
	v_pk_mul_f32 v[14:15], v[14:15], v[68:69] op_sel_hi:[1,0]
	v_pk_add_f32 v[70:71], v[132:133], v[70:71]
	v_pk_mul_f32 v[12:13], v[12:13], v[68:69] op_sel_hi:[1,0]
	v_cvt_pk_bf16_f32 v73, v82, v83
	v_cvt_pk_bf16_f32 v74, v168, v169
	v_cvt_pk_bf16_f32 v75, v96, v98
	v_pk_add_f32 v[70:71], v[134:135], v[70:71]
	s_waitcnt lgkmcnt(1)
; __device__ __forceinline__ float fexp2(float x) { return __builtin_amdgcn_exp2f(x); }
; #define MFMA32(a, b, c) __builtin_amdgcn_mfma_f32_16x16x32_bf16((a), (b), (c), 0, 0, 0)
; __device__ __forceinline__ bf16x8 cat8(bf16x4 a, bf16x4 b) { return __builtin_shufflevector(a, b, 0, 1, 2, 3, 4, 5, 6, 7); }
; __device__ void phase_swa_mfma(const Params& p, int l, char* smem, int vb, int nvb, int pend, int oz) {
;     ...
;                 float ps = 0.f;
; #pragma unroll
;                 for (int km = 0; km < 4; ++km)
; #pragma unroll
;                     for (int r = 0; r < 4; ++r) {
;                         const float pv = fexp2(st[km][qt2][r] - mn);
;                         st[km][qt2][r] = pv;
;                         ps += pv;
;                     }
;                 lsum[qt2] = lsum[qt2] * sc + ps;
; #pragma unroll
;                 for (int dt = 0; dt < 4; ++dt) O[dt][qt2] = O[dt][qt2] * sc;
;                 pf[qt2][0] = pack8(st[0][qt2], st[1][qt2]);
;                 pf[qt2][1] = pack8(st[2][qt2], st[3][qt2]);
;             }
; #pragma unroll
;             for (int dt = 0; dt < 4; ++dt)
; #pragma unroll
;                 for (int ks = 0; ks < 2; ++ks) {
;                     const bf16x8 va = cat8(lds_tr(Vl + (32 * ks + 4 * g + q4) * LS + 16 * dt + 4 * p4),
;                                            lds_tr(Vl + (32 * ks + 16 + 4 * g + q4) * LS + 16 * dt + 4 * p4));
; #pragma unroll
;                     for (int qt2 = 0; qt2 < 2; ++qt2) O[dt][qt2] = MFMA32(va, pf[qt2][ks], O[dt][qt2]);
;                 }
	v_mfma_f32_16x16x32_bf16 v[64:67], v[76:79], v[88:91], v[64:67]
	v_exp_f32_e32 v143, v84
	v_sub_f32_e32 v84, v95, v127
	v_pk_add_f32 v[70:71], v[136:137], v[70:71]
	v_mfma_f32_16x16x32_bf16 v[12:15], v[76:79], v[72:75], v[12:15]
	ds_read_b64_tr_b16 v[76:77], v165 offset:13824
	ds_read_b64_tr_b16 v[78:79], v165 offset:16128
	ds_read_b64_tr_b16 v[82:83], v165 offset:11552
	v_exp_f32_e32 v95, v84
	v_pk_add_f32 v[70:71], v[138:139], v[70:71]
	v_pk_mul_f32 v[86:87], v[54:55], v[146:147] op_sel_hi:[1,0]
	v_pk_add_f32 v[70:71], v[140:141], v[70:71]
	v_pk_mul_f32 v[84:85], v[52:53], v[146:147] op_sel_hi:[1,0]
	v_pk_add_f32 v[70:71], v[92:93], v[70:71]
	v_cvt_pk_bf16_f32 v52, v133, v135
	v_pk_add_f32 v[70:71], v[142:143], v[70:71]
	v_cvt_pk_bf16_f32 v53, v137, v139
	v_pk_add_f32 v[70:71], v[94:95], v[70:71]
	v_cvt_pk_bf16_f32 v54, v141, v93
	v_cvt_pk_bf16_f32 v55, v143, v95
	v_pk_fma_f32 v[130:131], v[130:131], v[68:69], v[70:71]
	v_pk_mul_f32 v[6:7], v[6:7], v[68:69] op_sel_hi:[1,0]
	v_pk_mul_f32 v[4:5], v[4:5], v[68:69] op_sel_hi:[1,0]
	v_pk_mul_f32 v[10:11], v[10:11], v[68:69] op_sel_hi:[1,0]
	v_pk_mul_f32 v[8:9], v[8:9], v[68:69] op_sel_hi:[1,0]
	v_pk_mul_f32 v[70:71], v[18:19], v[68:69] op_sel_hi:[1,0]
	v_pk_mul_f32 v[68:69], v[16:17], v[68:69] op_sel_hi:[1,0]
	v_cvt_pk_bf16_f32 v16, v132, v134
	v_cvt_pk_bf16_f32 v17, v136, v138
	v_cvt_pk_bf16_f32 v18, v140, v92
	v_cvt_pk_bf16_f32 v19, v142, v94
	v_pk_mul_f32 v[62:63], v[62:63], v[146:147] op_sel_hi:[1,0]
	v_pk_mul_f32 v[60:61], v[60:61], v[146:147] op_sel_hi:[1,0]
	s_waitcnt lgkmcnt(1)
	v_mfma_f32_16x16x32_bf16 v[64:67], v[76:79], v[52:55], v[64:67]
	v_mul_f32_e64 v58, v58, v146
	v_mul_f32_e64 v59, v59, v146
	v_pk_mul_f32 v[56:57], v[56:57], v[146:147] op_sel_hi:[1,0]
	v_mfma_f32_16x16x32_bf16 v[12:15], v[76:79], v[16:19], v[12:15]
	ds_read_b64_tr_b16 v[76:77], v165 offset:13856
	ds_read_b64_tr_b16 v[78:79], v165 offset:16160
	s_waitcnt lgkmcnt(2)
	v_mfma_f32_16x16x32_bf16 v[60:63], v[80:83], v[88:91], v[60:63]
	v_mfma_f32_16x16x32_bf16 v[4:7], v[80:83], v[72:75], v[4:7]
	s_waitcnt lgkmcnt(0)
	v_mfma_f32_16x16x32_bf16 v[60:63], v[76:79], v[52:55], v[60:63]
	v_mfma_f32_16x16x32_bf16 v[4:7], v[76:79], v[16:19], v[4:7]
	ds_read_b64_tr_b16 v[76:77], v165 offset:9280
	ds_read_b64_tr_b16 v[78:79], v165 offset:11584
	s_waitcnt lgkmcnt(0)
	v_mfma_f32_16x16x32_bf16 v[56:59], v[76:79], v[88:91], v[56:59]
	v_mfma_f32_16x16x32_bf16 v[8:11], v[76:79], v[72:75], v[8:11]
	ds_read_b64_tr_b16 v[76:77], v165 offset:13888
	ds_read_b64_tr_b16 v[78:79], v165 offset:16192
	s_waitcnt lgkmcnt(0)
	v_mfma_f32_16x16x32_bf16 v[56:59], v[76:79], v[52:55], v[56:59]
	v_mfma_f32_16x16x32_bf16 v[8:11], v[76:79], v[16:19], v[8:11]
	ds_read_b64_tr_b16 v[76:77], v165 offset:9312
	ds_read_b64_tr_b16 v[78:79], v165 offset:11616
	s_waitcnt lgkmcnt(0)
	v_mfma_f32_16x16x32_bf16 v[68:71], v[76:79], v[72:75], v[68:71]
	ds_read_b64_tr_b16 v[72:73], v165 offset:13920
	ds_read_b64_tr_b16 v[74:75], v165 offset:16224
	v_mfma_f32_16x16x32_bf16 v[80:83], v[76:79], v[88:91], v[84:87]
	s_waitcnt lgkmcnt(0)
	v_mfma_f32_16x16x32_bf16 v[52:55], v[72:75], v[52:55], v[80:83]
	v_mfma_f32_16x16x32_bf16 v[16:19], v[72:75], v[16:19], v[68:71]
	s_cbranch_scc1 .LBB0_178
	s_mov_b32 s24, s3
	v_mov_b32_e32 v121, v105
	v_mov_b32_e32 v105, v127
	s_branch .LBB0_192

; __global__ void __launch_bounds__(NT) fwd_megakernel(Params p) {
;     ...
;             const int n = vb & 3;
;             int m0, mc;
;             if (cls == 0) { const int j = vb >> 2; if (j < 26) { m0 = 3 * j; mc = 3; } else { m0 = 78 + 2 * (j - 26); mc = 2; } }
.LBB0_710:
	s_andn2_b64 vcc, exec, s[12:13]
	s_mov_b64 s[0:1], -1
	s_mov_b32 s80, s86
	s_waitcnt vmcnt(0) lgkmcnt(0)
	s_barrier
	s_cbranch_vccnz .LBB0_716
	s_ashr_i32 s3, s72, 2
	s_cmp_gt_i32 s3, 31
	s_cbranch_scc0 .LBB0_713
	s_lshl_b32 s0, s3, 1
	s_add_i32 s21, s0, 32
	s_mov_b64 s[0:1], 0

; __global__ void __launch_bounds__(NT) fwd_megakernel(Params p) {
;     ...
;             else if (cls == 1) { const int j = (vb - 160) >> 2; if (j < 6) { m0 = 106 + 7 * j; mc = 7; } else { m0 = 148 + 6 * (j - 6); mc = 6; } }
;             else { const int j = (vb - 224) >> 2; m0 = 208 + 10 * j; mc = 10; }
;             lru_loop<0>(p, l, smem, n + 4 * m0, n + 4 * (m0 + mc), 4, false, oz);
.LBB0_719:
	s_andn2_b64 vcc, exec, s[0:1]
	s_mov_b32 s2, 10
	s_cbranch_vccnz .LBB0_724
	s_lshr_b32 s3, s9, 2
	s_cmp_ge_u32 s9, 0
	s_mov_b64 s[0:1], -1
	s_cbranch_scc0 .LBB0_722
	s_mul_i32 s0, s3, 6
	s_add_i32 s21, s0, 0x70
	s_mov_b64 s[0:1], 0
